# grid barrier: early unwaited write-back at arrival (pre-flush)
# baseline (speedup 1.0000x reference)
.LBB0_139:
	v_readlane_b32 s6, v255, 4
	v_readlane_b32 s7, v255, 5
	s_lshl_b64 s[6:7], s[6:7], 2
	v_readlane_b32 s3, v255, 2
	s_add_u32 s8, s3, s6
	v_readlane_b32 s3, v255, 3
	s_addc_u32 s9, s3, s7
	v_readlane_b32 s3, v255, 6
	s_lshl_b32 s3, s3, 8
	s_add_u32 s6, s8, s3
	s_addc_u32 s7, s9, 0
	v_mov_b32_e32 v2, 0x1000
	v_mov_b32_e32 v4, 1
	global_atomic_add v4, v2, v4, s[6:7] offset:1024 sc0
	buffer_inv sc1
	buffer_wbl2 sc1
	v_cvt_f32_u32_e32 v2, v3
	v_sub_u32_e32 v5, 0, v3
	v_rcp_iflag_f32_e32 v2, v2
	s_nop 0
	v_mul_f32_e32 v2, 0x4f7ffffe, v2
	v_cvt_u32_f32_e32 v2, v2
	v_mul_lo_u32 v5, v5, v2
	v_mul_hi_u32 v5, v2, v5
	v_add_u32_e32 v2, v2, v5
	s_waitcnt vmcnt(2)
	v_mul_hi_u32 v2, v4, v2
	v_mul_lo_u32 v5, v2, v3
	v_sub_u32_e32 v5, v4, v5
	v_add_u32_e32 v6, 1, v2
	v_cmp_ge_u32_e32 vcc, v5, v3
	v_add_u32_e32 v4, 1, v4
	s_nop 0
	v_cndmask_b32_e32 v2, v2, v6, vcc
	v_sub_u32_e32 v6, v5, v3
	v_cndmask_b32_e32 v5, v5, v6, vcc
	v_add_u32_e32 v6, 1, v2
	v_cmp_ge_u32_e32 vcc, v5, v3
	s_nop 1
	v_cndmask_b32_e32 v2, v2, v6, vcc
	v_mul_lo_u32 v5, v3, v2
	v_add_u32_e32 v3, v5, v3
	v_cmp_ne_u32_e32 vcc, v4, v3
	s_and_saveexec_b64 s[12:13], vcc
	s_xor_b64 s[12:13], exec, s[12:13]
	s_cbranch_execz .LBB0_153
	s_waitcnt lgkmcnt(0)
	v_mov_b32_e32 v1, 0x2000
	global_load_dword v1, v1, s[6:7] offset:1024 sc1
	s_add_u32 s16, s6, 0x2400
	s_addc_u32 s17, s7, 0
	s_waitcnt vmcnt(0)
	v_cmp_eq_u32_e32 vcc, v1, v2
	s_and_saveexec_b64 s[14:15], vcc
	s_cbranch_execz .LBB0_152
	s_mov_b32 s3, 1
	s_mov_b64 s[18:19], 0
	v_mov_b32_e32 v1, 0
	s_branch .LBB0_143

.LBB0_193:
	v_readlane_b32 s6, v255, 4
	v_readlane_b32 s7, v255, 5
	s_lshl_b64 s[6:7], s[6:7], 2
	v_readlane_b32 s3, v255, 2
	s_add_u32 s8, s3, s6
	v_readlane_b32 s3, v255, 3
	s_addc_u32 s9, s3, s7
	v_readlane_b32 s3, v255, 6
	s_lshl_b32 s3, s3, 8
	s_add_u32 s6, s8, s3
	s_addc_u32 s7, s9, 0
	v_mov_b32_e32 v2, 0x1000
	v_mov_b32_e32 v4, 1
	global_atomic_add v4, v2, v4, s[6:7] offset:1024 sc0
	buffer_inv sc1
	buffer_wbl2 sc1
	v_cvt_f32_u32_e32 v2, v3
	v_sub_u32_e32 v5, 0, v3
	v_rcp_iflag_f32_e32 v2, v2
	s_nop 0
	v_mul_f32_e32 v2, 0x4f7ffffe, v2
	v_cvt_u32_f32_e32 v2, v2
	v_mul_lo_u32 v5, v5, v2
	v_mul_hi_u32 v5, v2, v5
	v_add_u32_e32 v2, v2, v5
	s_waitcnt vmcnt(2)
	v_mul_hi_u32 v2, v4, v2
	v_mul_lo_u32 v5, v2, v3
	v_sub_u32_e32 v5, v4, v5
	v_add_u32_e32 v6, 1, v2
	v_cmp_ge_u32_e32 vcc, v5, v3
	v_add_u32_e32 v4, 1, v4
	s_nop 0
	v_cndmask_b32_e32 v2, v2, v6, vcc
	v_sub_u32_e32 v6, v5, v3
	v_cndmask_b32_e32 v5, v5, v6, vcc
	v_add_u32_e32 v6, 1, v2
	v_cmp_ge_u32_e32 vcc, v5, v3
	s_nop 1
	v_cndmask_b32_e32 v2, v2, v6, vcc
	v_mul_lo_u32 v5, v3, v2
	v_add_u32_e32 v3, v5, v3
	v_cmp_ne_u32_e32 vcc, v4, v3
	s_and_saveexec_b64 s[10:11], vcc
	s_xor_b64 s[10:11], exec, s[10:11]
	s_cbranch_execz .LBB0_207
	s_waitcnt lgkmcnt(0)
	v_mov_b32_e32 v1, 0x2000
	global_load_dword v1, v1, s[6:7] offset:1024 sc1
	s_add_u32 s14, s6, 0x2400
	s_addc_u32 s15, s7, 0
	s_waitcnt vmcnt(0)
	v_cmp_eq_u32_e32 vcc, v1, v2
	s_and_saveexec_b64 s[12:13], vcc
	s_cbranch_execz .LBB0_206
	s_mov_b32 s3, 1
	s_mov_b64 s[16:17], 0
	v_mov_b32_e32 v1, 0
	s_branch .LBB0_197

.LBB0_3030:
	v_readlane_b32 s4, v255, 4
	v_readlane_b32 s5, v255, 5
	s_lshl_b64 s[4:5], s[4:5], 2
	v_readlane_b32 s6, v255, 2
	s_add_u32 s6, s6, s4
	v_readlane_b32 s4, v255, 3
	s_addc_u32 s7, s4, s5
	v_readlane_b32 s4, v255, 6
	s_lshl_b32 s4, s4, 8
	s_add_u32 s4, s6, s4
	s_addc_u32 s5, s7, 0
	v_mov_b32_e32 v1, 0x1000
	v_mov_b32_e32 v3, 1
	global_atomic_add v3, v1, v3, s[4:5] offset:1024 sc0
	buffer_inv sc1
	buffer_wbl2 sc1
	v_cvt_f32_u32_e32 v1, v2
	v_sub_u32_e32 v4, 0, v2
	v_rcp_iflag_f32_e32 v1, v1
	s_nop 0
	v_mul_f32_e32 v1, 0x4f7ffffe, v1
	v_cvt_u32_f32_e32 v1, v1
	v_mul_lo_u32 v4, v4, v1
	v_mul_hi_u32 v4, v1, v4
	v_add_u32_e32 v1, v1, v4
	s_waitcnt vmcnt(2)
	v_mul_hi_u32 v1, v3, v1
	v_mul_lo_u32 v4, v1, v2
	v_sub_u32_e32 v4, v3, v4
	v_add_u32_e32 v5, 1, v1
	v_cmp_ge_u32_e32 vcc, v4, v2
	v_add_u32_e32 v3, 1, v3
	s_nop 0
	v_cndmask_b32_e32 v1, v1, v5, vcc
	v_sub_u32_e32 v5, v4, v2
	v_cndmask_b32_e32 v4, v4, v5, vcc
	v_add_u32_e32 v5, 1, v1
	v_cmp_ge_u32_e32 vcc, v4, v2
	s_nop 1
	v_cndmask_b32_e32 v1, v1, v5, vcc
	v_mul_lo_u32 v4, v2, v1
	v_add_u32_e32 v2, v4, v2
	v_cmp_ne_u32_e32 vcc, v3, v2
	s_and_saveexec_b64 s[8:9], vcc
	s_xor_b64 s[8:9], exec, s[8:9]
	s_cbranch_execz .LBB0_3044
	s_waitcnt lgkmcnt(0)
	v_mov_b32_e32 v0, 0x2000
	global_load_dword v0, v0, s[4:5] offset:1024 sc1
	s_add_u32 s12, s4, 0x2400
	s_addc_u32 s13, s5, 0
	s_waitcnt vmcnt(0)
	v_cmp_eq_u32_e32 vcc, v0, v1
	s_and_saveexec_b64 s[10:11], vcc
	s_cbranch_execz .LBB0_3043
	s_mov_b32 s28, 1
	s_mov_b64 s[14:15], 0
	v_mov_b32_e32 v0, 0
	s_branch .LBB0_3034
